# plus: MLA latent attention fetches K tiles as whole 128-byte key rows (8 rows per wave instruction) into a swizzled row-major LDS image
# speedup vs baseline: 1.0054x; 1.0054x over previous
.LBB0_1444:
	s_mul_i32 s26, s0, 0x440000
	s_mul_hi_i32 s9, s0, 0x440000
	s_add_u32 s2, s72, s26
	s_addc_u32 s3, s73, s9
	s_lshl_b32 s27, s29, 7
	s_add_u32 s2, s2, s27
	s_addc_u32 s3, s3, 0
	s_mul_hi_i32 s7, s0, 0x44000
	s_mul_i32 s0, s0, 0x44000
	s_add_u32 s6, s74, s0
	s_addc_u32 s7, s75, s7
	v_and_b32_e32 v164, 63, v54
	s_add_u32 s0, s76, s26
	s_addc_u32 s9, s77, s9
	v_lshlrev_b32_e32 v2, 10, v164
	s_add_u32 s36, s0, s27
	v_lshl_add_u64 v[6:7], s[2:3], 0, v[2:3]
	v_lshlrev_b32_e32 v2, 8, v164
	s_addc_u32 s37, s9, 0
	s_lshl_b32 s62, s8, 3
	v_lshlrev_b32_e32 v4, 6, v164
	v_mov_b32_e32 v5, v3
	s_and_b32 s0, s8, 3
	s_ashr_i32 s9, s1, 3
	v_and_b32_e32 v2, 0x3c00, v2
	s_ashr_i32 s63, s62, 31
	s_and_b32 s78, s9, 0xffffffe0
	v_lshlrev_b32_e32 v165, 3, v54
	s_lshl_b32 s9, s8, 10
	s_lshl_b32 s27, s0, 10
	v_lshl_add_u64 v[4:5], s[6:7], 0, v[4:5]
	s_lshl_b32 s92, s0, 4
	v_lshl_or_b32 v2, s0, 14, v2
	s_ashr_i32 s79, s78, 31
	v_and_b32_e32 v37, 24, v165
	s_add_i32 s9, s9, 0
	v_lshl_add_u64 v[68:69], s[62:63], 1, v[6:7]
	v_lshrrev_b32_e32 v240, 3, v164
	s_lshl_b32 s62, s8, 3
	v_add_u32_e32 v240, s62, v240
	v_lshlrev_b32_e32 v241, 10, v240
	v_bfe_u32 v242, v164, 4, 2
	s_and_b32 s62, s8, 1
	s_lshl_b32 s62, s62, 2
	v_or_b32_e32 v242, s62, v242
	v_and_b32_e32 v243, 7, v164
	v_xor_b32_e32 v242, v243, v242
	v_lshl_add_u32 v242, v242, 4, v241
	v_mov_b32_e32 v243, 0
	v_lshl_add_u64 v[68:69], s[2:3], 0, v[242:243]
	v_lshl_add_u64 v[70:71], v[4:5], 0, s[92:93]
	v_lshl_add_u64 v[4:5], s[36:37], 0, v[2:3]
	s_add_i32 s27, s27, 0
	s_mov_b32 s0, m0
	s_mov_b32 m0, s9
	s_nop 0
	global_load_lds_dwordx4 v[68:69], off
	s_mov_b32 m0, s0
	v_lshl_add_u64 v[4:5], s[78:79], 1, v[4:5]
	v_lshlrev_b32_e32 v2, 1, v37
	s_addk_i32 s27, 0x2000
	s_mov_b32 s0, m0
	s_mov_b32 m0, s27
	s_nop 0
	global_load_lds_dwordx4 v[70:71], off
	s_mov_b32 m0, s0
	s_add_i32 s26, s9, 0xc000
	v_lshl_add_u64 v[72:73], v[4:5], 0, v[2:3]
	s_mov_b32 s0, m0
	s_mov_b32 m0, s26
	s_nop 0
	global_load_lds_dwordx4 v[72:73], off
	s_mov_b32 m0, s0
	s_mov_b64 s[6:7], 0x10000
	v_lshl_add_u64 v[4:5], v[68:69], 0, s[6:7]
	s_add_i32 s0, s9, 0x3000
	s_mov_b32 s2, m0
	s_mov_b32 m0, s0
	s_nop 0
	global_load_lds_dwordx4 v[4:5], off
	s_mov_b32 m0, s2
	s_mov_b64 s[2:3], 0x1000
	v_lshl_add_u64 v[4:5], v[70:71], 0, s[2:3]
	s_add_i32 s0, s27, 0x3000
	s_mov_b32 s2, m0
	s_mov_b32 m0, s0
	s_nop 0
	global_load_lds_dwordx4 v[4:5], off
	s_mov_b32 m0, s2
	v_lshl_add_u64 v[4:5], v[72:73], 0, s[6:7]
	s_add_i32 s0, s26, 0x2000
	s_mov_b32 s2, m0
	s_mov_b32 m0, s0
	s_nop 0
	global_load_lds_dwordx4 v[4:5], off
	s_mov_b32 m0, s2
	v_lshl_add_u64 v[4:5], v[68:69], 0, s[84:85]
	s_add_i32 s0, s9, 0x6000
	s_mov_b32 s2, m0
	s_mov_b32 m0, s0
	s_nop 0
	global_load_lds_dwordx4 v[4:5], off
	s_mov_b32 m0, s2
	v_lshl_add_u64 v[4:5], v[70:71], 0, s[96:97]
	s_add_i32 s0, s27, 0x6000
	s_mov_b32 s2, m0
	s_mov_b32 m0, s0
	s_nop 0
	global_load_lds_dwordx4 v[4:5], off
	s_mov_b32 m0, s2
	v_lshl_add_u64 v[4:5], v[72:73], 0, s[84:85]
	s_add_i32 s0, s26, 0x4000
	s_mov_b32 s2, m0
	s_mov_b32 m0, s0
	s_nop 0
	global_load_lds_dwordx4 v[4:5], off
	s_mov_b32 m0, s2
	v_lshlrev_b32_e32 v2, 10, v167
	v_lshlrev_b32_e32 v4, 4, v166
	v_add3_u32 v168, 0, v2, v4
	v_bfe_u32 v240, v166, 1, 3
	v_lshlrev_b32_e32 v241, 7, v166
	v_or_b32_e32 v242, 0, v167
	v_xor_b32_e32 v242, v242, v240
	v_lshl_add_u32 v244, v242, 4, v241
	v_or_b32_e32 v242, 2, v167
	v_xor_b32_e32 v242, v242, v240
	v_lshl_add_u32 v245, v242, 4, v241
	v_or_b32_e32 v242, 4, v167
	v_xor_b32_e32 v242, v242, v240
	v_lshl_add_u32 v246, v242, 4, v241
	v_or_b32_e32 v242, 6, v167
	v_xor_b32_e32 v242, v242, v240
	v_lshl_add_u32 v247, v242, 4, v241
	s_waitcnt vmcnt(6) lgkmcnt(0)
	s_barrier
	ds_read_b128 v[4:7], v244
	s_waitcnt vmcnt(0) lgkmcnt(0)
	v_mfma_f32_32x32x16_bf16 v[38:53], v[4:7], v[116:119], 0
	ds_read_b128 v[4:7], v244 offset:4096
	s_and_b32 s0, s1, 0x3fffffc0
	s_lshl_b32 s0, s0, 2
	s_add_i32 s28, s0, 0
	s_mov_b32 s0, 0xf149f2ca
	s_add_i32 s28, s28, 0x14000
	s_waitcnt lgkmcnt(0)
	v_mfma_f32_32x32x16_bf16 v[20:35], v[4:7], v[116:119], 0
	ds_read_b128 v[4:7], v245
	s_waitcnt lgkmcnt(0)
	v_mfma_f32_32x32x16_bf16 v[38:53], v[4:7], v[120:123], v[38:53]
	ds_read_b128 v[4:7], v245 offset:4096
	s_waitcnt lgkmcnt(0)
	v_mfma_f32_32x32x16_bf16 v[20:35], v[4:7], v[120:123], v[20:35]
	ds_read_b128 v[4:7], v246
	s_waitcnt lgkmcnt(0)
	v_mfma_f32_32x32x16_bf16 v[38:53], v[4:7], v[124:127], v[38:53]
	ds_read_b128 v[4:7], v246 offset:4096
	s_waitcnt lgkmcnt(0)
	v_mfma_f32_32x32x16_bf16 v[20:35], v[4:7], v[124:127], v[20:35]
	ds_read_b128 v[4:7], v247
	s_waitcnt lgkmcnt(0)
	v_mfma_f32_32x32x16_bf16 v[38:53], v[4:7], v[128:131], v[38:53]
	ds_read_b128 v[4:7], v247 offset:4096
	s_waitcnt lgkmcnt(0)
	v_mfma_f32_32x32x16_bf16 v[20:35], v[4:7], v[128:131], v[20:35]
	ds_read_b128 v[4:7], v168 offset:8192
	s_waitcnt lgkmcnt(0)
	v_mfma_f32_32x32x16_bf16 v[38:53], v[4:7], v[132:135], v[38:53]
	ds_read_b128 v[4:7], v168 offset:8704
	s_waitcnt lgkmcnt(0)
	v_mfma_f32_32x32x16_bf16 v[20:35], v[4:7], v[132:135], v[20:35]
	ds_read_b128 v[4:7], v168 offset:10240
	s_waitcnt lgkmcnt(0)
	v_mfma_f32_32x32x16_bf16 v[38:53], v[4:7], v[136:139], v[38:53]
	ds_read_b128 v[4:7], v168 offset:10752
	s_waitcnt lgkmcnt(0)
	v_mfma_f32_32x32x16_bf16 v[20:35], v[4:7], v[136:139], v[20:35]
	s_nop 8
	v_max_f32_e32 v4, v39, v39
	v_max_f32_e32 v5, v40, v40
	v_max_f32_e32 v6, v41, v41
	v_max_f32_e32 v2, v21, v21
	v_max_f32_e32 v2, v4, v2
	v_max_f32_e32 v4, v22, v22
	v_max_f32_e32 v4, v5, v4
	v_max_f32_e32 v5, v23, v23
	v_max3_f32 v2, v38, v20, v2
	v_max_f32_e32 v5, v6, v5
	v_max3_f32 v2, v2, v4, v5
	v_max_f32_e32 v4, v24, v24
	v_max_f32_e32 v5, v42, v42
	v_max_f32_e32 v4, v5, v4
	v_max_f32_e32 v5, v25, v25
	v_max_f32_e32 v6, v43, v43
	v_max_f32_e32 v5, v6, v5
	v_max3_f32 v2, v2, v4, v5
	v_max_f32_e32 v4, v26, v26
	v_max_f32_e32 v5, v44, v44
	v_max_f32_e32 v4, v5, v4
	v_max_f32_e32 v5, v27, v27
	v_max_f32_e32 v6, v45, v45
	v_max_f32_e32 v5, v6, v5
	v_max3_f32 v2, v2, v4, v5
	v_max_f32_e32 v4, v28, v28
	v_max_f32_e32 v5, v46, v46
	v_max_f32_e32 v4, v5, v4
	v_max_f32_e32 v5, v29, v29
	v_max_f32_e32 v6, v47, v47
	v_max_f32_e32 v5, v6, v5
	v_max3_f32 v2, v2, v4, v5
	v_max_f32_e32 v4, v30, v30
	v_max_f32_e32 v5, v48, v48
	v_max_f32_e32 v4, v5, v4
	v_max_f32_e32 v5, v31, v31
	v_max_f32_e32 v6, v49, v49
	v_max_f32_e32 v5, v6, v5
	v_max3_f32 v2, v2, v4, v5
	v_max_f32_e32 v4, v32, v32
	v_max_f32_e32 v5, v50, v50
	v_max_f32_e32 v4, v5, v4
	v_max_f32_e32 v5, v33, v33
	v_max_f32_e32 v6, v51, v51
	v_max_f32_e32 v5, v6, v5
	v_max3_f32 v2, v2, v4, v5
	v_max_f32_e32 v4, v34, v34
	v_max_f32_e32 v5, v52, v52
	v_max_f32_e32 v4, v5, v4
	v_max_f32_e32 v5, v35, v35
	v_max_f32_e32 v6, v53, v53
	v_max_f32_e32 v5, v6, v5
	v_max3_f32 v2, v2, v4, v5
	v_mov_b32_e32 v4, v2
	s_nop 1
	v_permlane32_swap_b32_e32 v2, v4
	v_max_f32_e32 v4, v4, v4
	v_max_f32_e32 v2, v2, v2
	v_max_f32_e32 v2, v2, v4
	v_cmp_lt_f32_e32 vcc, s0, v2
	v_cmp_gt_u32_e64 s[0:1], 32, v164
	s_cbranch_vccz .LBB0_1534
	v_max_f32_e32 v2, v2, v2
	v_max_f32_e32 v74, 0xf149f2ca, v2
	v_sub_f32_e32 v2, 0xf149f2ca, v74
	v_exp_f32_e32 v2, v2
	s_and_saveexec_b64 s[6:7], s[0:1]
	v_lshl_add_u32 v4, v166, 2, s28
	ds_write_b32 v4, v2
	s_or_b64 exec, exec, s[6:7]
	v_lshlrev_b32_e32 v169, 4, v167
	s_waitcnt lgkmcnt(0)
	v_add_u32_e32 v12, s28, v169
	ds_read_b128 v[4:7], v12 offset:96
	ds_read_b128 v[8:11], v12 offset:64
	ds_read_b128 v[56:59], v12 offset:32
	ds_read_b128 v[60:63], v12
	s_waitcnt lgkmcnt(0)
	v_mul_f32_e32 v171, 0, v2
	s_waitcnt lgkmcnt(3)
	v_pk_mul_f32 v[18:19], v[6:7], 0 op_sel_hi:[1,0]
	s_waitcnt lgkmcnt(2)
	v_pk_mul_f32 v[14:15], v[10:11], 0 op_sel_hi:[1,0]
	s_waitcnt lgkmcnt(1)
	v_pk_mul_f32 v[10:11], v[58:59], 0 op_sel_hi:[1,0]
	s_waitcnt lgkmcnt(0)
	v_pk_mul_f32 v[6:7], v[62:63], 0 op_sel_hi:[1,0]
	v_pk_mul_f32 v[16:17], v[4:5], 0 op_sel_hi:[1,0]
	v_pk_mul_f32 v[12:13], v[8:9], 0 op_sel_hi:[1,0]
	v_pk_mul_f32 v[8:9], v[56:57], 0 op_sel_hi:[1,0]
	v_pk_mul_f32 v[4:5], v[60:61], 0 op_sel_hi:[1,0]
	s_branch .LBB0_1449

.LBB0_1456:
	s_add_i32 s2, s79, 1
	s_and_b32 s2, s2, 3
	s_mulk_i32 s2, 0x3000
	v_add_u32_e32 v72, s2, v168
	v_add_u32_e32 v248, s2, v244
	v_add_u32_e32 v249, s2, v245
	v_add_u32_e32 v250, s2, v246
	v_add_u32_e32 v251, s2, v247
	ds_read_b128 v[68:71], v248
	ds_read_b128 v[172:175], v248 offset:4096
	ds_read_b128 v[176:179], v249
	ds_read_b128 v[180:183], v249 offset:4096
	ds_read_b128 v[184:187], v250
	ds_read_b128 v[190:193], v250 offset:4096
	ds_read_b128 v[212:215], v251
	ds_read_b128 v[216:219], v251 offset:4096
	ds_read_b128 v[224:227], v72 offset:8192
	ds_read_b128 v[228:231], v72 offset:8704
	ds_read_b128 v[232:235], v72 offset:10240
	ds_read_b128 v[236:239], v72 offset:10752
	s_waitcnt lgkmcnt(11)
	v_mfma_f32_32x32x16_bf16 v[100:115], v[68:71], v[116:119], v[36:51]
	v_exp_f32_e32 v84, v84
	v_exp_f32_e32 v85, v85
	v_exp_f32_e32 v86, v86
	v_exp_f32_e32 v87, v87
	s_waitcnt lgkmcnt(10)
	v_mfma_f32_32x32x16_bf16 v[68:83], v[172:175], v[116:119], v[36:51]
	v_add_f32_e64 v172, v84, 0
	v_add_f32_e64 v173, v85, 0
	v_add_f32_e64 v172, v86, v172
	v_add_f32_e64 v173, v87, v173
	s_waitcnt lgkmcnt(9)
	v_mfma_f32_32x32x16_bf16 v[100:115], v[176:179], v[120:123], v[100:115]
	v_exp_f32_e32 v88, v88
	v_exp_f32_e32 v89, v89
	v_exp_f32_e32 v90, v90
	v_exp_f32_e32 v91, v91
	v_pk_add_f32 v[172:173], v[88:89], v[172:173]
	s_nop 0
	v_pk_add_f32 v[172:173], v[90:91], v[172:173]
	s_waitcnt lgkmcnt(8)
	v_mfma_f32_32x32x16_bf16 v[68:83], v[180:183], v[120:123], v[68:83]
	s_waitcnt lgkmcnt(7)
	v_mfma_f32_32x32x16_bf16 v[100:115], v[184:187], v[124:127], v[100:115]
	v_exp_f32_e32 v92, v92
	v_exp_f32_e32 v93, v93
	v_exp_f32_e32 v94, v94
	v_exp_f32_e32 v95, v95
	v_pk_add_f32 v[172:173], v[92:93], v[172:173]
	s_nop 0
	v_pk_add_f32 v[172:173], v[94:95], v[172:173]
	s_waitcnt lgkmcnt(6)
	v_mfma_f32_32x32x16_bf16 v[68:83], v[190:193], v[124:127], v[68:83]
	s_waitcnt lgkmcnt(5)
	v_mfma_f32_32x32x16_bf16 v[100:115], v[212:215], v[128:131], v[100:115]
	v_exp_f32_e32 v96, v96
	v_exp_f32_e32 v97, v97
	v_exp_f32_e32 v98, v98
	v_exp_f32_e32 v99, v99
	v_pk_add_f32 v[172:173], v[96:97], v[172:173]
	s_nop 0
	v_pk_add_f32 v[172:173], v[98:99], v[172:173]
	s_waitcnt lgkmcnt(4)
	v_mfma_f32_32x32x16_bf16 v[68:83], v[216:219], v[128:131], v[68:83]
	v_exp_f32_e32 v174, v52
	v_exp_f32_e32 v175, v53
	s_waitcnt lgkmcnt(3)
	v_mfma_f32_32x32x16_bf16 v[100:115], v[224:227], v[132:135], v[100:115]
	v_add_f32_e64 v52, v174, v172
	v_add_f32_e64 v53, v175, v173
	v_exp_f32_e32 v172, v54
	v_exp_f32_e32 v173, v55
	s_nop 0
	v_pk_add_f32 v[52:53], v[172:173], v[52:53]
	s_waitcnt lgkmcnt(2)
	v_mfma_f32_32x32x16_bf16 v[68:83], v[228:231], v[132:135], v[68:83]
	s_waitcnt lgkmcnt(1)
	v_mfma_f32_32x32x16_bf16 v[100:115], v[232:235], v[136:139], v[100:115]
	v_exp_f32_e32 v176, v56
	v_exp_f32_e32 v177, v57
	v_exp_f32_e32 v178, v58
	v_exp_f32_e32 v179, v59
	v_pk_add_f32 v[52:53], v[176:177], v[52:53]
	s_nop 0
	v_pk_add_f32 v[194:195], v[178:179], v[52:53]
	s_waitcnt lgkmcnt(0)
	v_mfma_f32_32x32x16_bf16 v[68:83], v[236:239], v[136:139], v[68:83]
	s_and_b32 s2, s78, 0x4000
	v_cvt_pk_bf16_f32 v54, v88, v89
	v_add_u32_e32 v212, s2, v2
	ds_read_b64_tr_b16 v[88:89],v212 offset:0
	v_cvt_pk_bf16_f32 v55, v90, v91
	ds_read_b64_tr_b16 v[90:91],v212 offset:512
	v_cvt_pk_bf16_f32 v56, v92, v93
	ds_read_b64_tr_b16 v[92:93],v212 offset:1024
	v_cvt_pk_bf16_f32 v57, v94, v95
	ds_read_b64_tr_b16 v[94:95],v212 offset:1536
	v_cvt_pk_bf16_f32 v58, v96, v97
	ds_read_b64_tr_b16 v[96:97],v212 offset:2048
	v_cvt_pk_bf16_f32 v59, v98, v99
	ds_read_b64_tr_b16 v[98:99],v212 offset:2560
	v_cvt_pk_bf16_f32 v52, v84, v85
	v_cvt_pk_bf16_f32 v85, v172, v173
	ds_read_b64_tr_b16 v[172:173],v212 offset:3072
	v_cvt_pk_bf16_f32 v84, v174, v175
	ds_read_b64_tr_b16 v[174:175],v212 offset:3584
	v_cvt_pk_bf16_f32 v53, v86, v87
	v_cvt_pk_bf16_f32 v86, v176, v177
	ds_read_b64_tr_b16 v[176:177],v212 offset:4096
	v_cvt_pk_bf16_f32 v87, v178, v179
	ds_read_b64_tr_b16 v[178:179],v212 offset:4608
	ds_read_b64_tr_b16 v[180:181],v212 offset:5120
	ds_read_b64_tr_b16 v[182:183],v212 offset:5632
	ds_read_b64_tr_b16 v[184:185],v212 offset:6144
	ds_read_b64_tr_b16 v[186:187],v212 offset:6656
	ds_read_b64_tr_b16 v[190:191],v212 offset:7168
	ds_read_b64_tr_b16 v[192:193],v212 offset:7680
	s_waitcnt lgkmcnt(0)
	v_mfma_f32_32x32x16_bf16 v[4:19], v[52:55], v[88:91], v[4:19]
	v_mfma_f32_32x32x16_bf16 v[20:35], v[52:55], v[176:179], v[20:35]
	v_exp_f32_e32 v52, v60
	v_exp_f32_e32 v53, v61
	v_exp_f32_e32 v60, v62
	v_exp_f32_e32 v61, v63
	v_pk_add_f32 v[54:55], v[52:53], v[194:195]
	s_nop 0
	v_pk_add_f32 v[54:55], v[60:61], v[54:55]
	v_mfma_f32_32x32x16_bf16 v[4:19], v[56:59], v[92:95], v[4:19]
	v_cvt_pk_bf16_f32 v52, v52, v53
	v_cvt_pk_bf16_f32 v53, v60, v61
	v_mfma_f32_32x32x16_bf16 v[20:35], v[56:59], v[180:183], v[20:35]
	v_exp_f32_e32 v56, v64
	v_exp_f32_e32 v57, v65
	v_exp_f32_e32 v58, v66
	v_exp_f32_e32 v59, v67
	v_pk_add_f32 v[54:55], v[56:57], v[54:55]
	s_nop 0
	v_pk_add_f32 v[62:63], v[58:59], v[54:55]
	v_cvt_pk_bf16_f32 v54, v56, v57
	v_add_f32_e32 v56, v62, v63
	v_add_f32_e32 v171, v171, v56
	v_cvt_pk_bf16_f32 v55, v58, v59
	v_mfma_f32_32x32x16_bf16 v[4:19], v[84:87], v[96:99], v[4:19]
	v_max3_f32 v56, v100, v68, v101
	s_nop 0
	v_max3_f32 v56, v56, v69, v102
	s_nop 0
	v_max3_f32 v56, v56, v70, v103
	s_nop 0
	v_max3_f32 v56, v56, v71, v104
	v_mfma_f32_32x32x16_bf16 v[20:35], v[84:87], v[184:187], v[20:35]
	v_max3_f32 v56, v56, v72, v105
	s_nop 0
	v_max3_f32 v56, v56, v73, v106
	s_nop 0
	v_max3_f32 v56, v56, v74, v107
	s_nop 0
	v_max3_f32 v56, v56, v75, v107
	v_mfma_f32_32x32x16_bf16 v[4:19], v[52:55], v[172:175], v[4:19]
	v_mfma_f32_32x32x16_bf16 v[20:35], v[52:55], v[190:193], v[20:35]
	v_max3_f32 v52, v56, v108, v76
	s_nop 0
	v_max3_f32 v52, v52, v109, v77
	s_nop 0
	v_max3_f32 v52, v52, v110, v78
	s_nop 0
	v_max3_f32 v52, v52, v111, v79
	s_nop 0
	v_max3_f32 v52, v52, v112, v80
	s_nop 0
	v_max3_f32 v52, v52, v113, v81
	s_nop 0
	v_max3_f32 v52, v52, v114, v82
	s_nop 0
	v_max3_f32 v52, v52, v115, v83
	s_nop 0
	v_mov_b32_e32 v53, v52
	s_nop 1
	v_permlane32_swap_b32_e32 v52, v53
	v_max_f32_e32 v53, v53, v53
	v_max_f32_e32 v52, v52, v52
	v_max_f32_e32 v52, v52, v53
	v_cmp_lt_f32_e32 vcc, s13, v52
	s_cbranch_vccz .LBB0_1460
	v_max_f32_e32 v52, v52, v52
	v_max_f32_e32 v52, 0, v52
	v_exp_f32_e64 v53, -v52
	s_and_saveexec_b64 s[6:7], s[36:37]
	ds_write_b32 v170, v53
	s_or_b64 exec, exec, s[6:7]
	v_mul_f32_e32 v171, v171, v53
	s_waitcnt lgkmcnt(0)
	v_add_u32_e32 v53, s28, v169
	ds_read_b128 v[54:57], v53
	ds_read_b128 v[58:61], v53 offset:32
	ds_read_b128 v[62:65], v53 offset:64
	ds_read_b128 v[84:87], v53 offset:96
	s_waitcnt lgkmcnt(0)
	s_waitcnt lgkmcnt(3)
	v_pk_mul_f32 v[6:7], v[6:7], v[56:57]
	s_waitcnt lgkmcnt(2)
	v_pk_mul_f32 v[8:9], v[8:9], v[58:59]
	s_waitcnt lgkmcnt(1)
	v_pk_mul_f32 v[12:13], v[12:13], v[62:63]
	s_waitcnt lgkmcnt(0)
	v_pk_mul_f32 v[16:17], v[16:17], v[84:85]
	v_pk_mul_f32 v[18:19], v[18:19], v[86:87]
	v_pk_mul_f32 v[14:15], v[14:15], v[64:65]
	v_pk_mul_f32 v[10:11], v[10:11], v[60:61]
	v_pk_mul_f32 v[4:5], v[4:5], v[54:55]
	v_pk_mul_f32 v[32:33], v[32:33], v[84:85]
	v_pk_mul_f32 v[28:29], v[28:29], v[62:63]
	v_pk_mul_f32 v[24:25], v[24:25], v[58:59]
	v_pk_mul_f32 v[34:35], v[34:35], v[86:87]
	v_pk_mul_f32 v[30:31], v[30:31], v[64:65]
	v_pk_mul_f32 v[26:27], v[26:27], v[60:61]
	v_pk_mul_f32 v[22:23], v[22:23], v[56:57]
	v_pk_mul_f32 v[20:21], v[20:21], v[54:55]
	v_sub_f32_e32 v115, v115, v52
	v_sub_f32_e32 v114, v114, v52
	v_sub_f32_e32 v113, v113, v52
	v_sub_f32_e32 v112, v112, v52
	v_sub_f32_e32 v111, v111, v52
	v_sub_f32_e32 v110, v110, v52
	v_sub_f32_e32 v109, v109, v52
	v_sub_f32_e32 v108, v108, v52
	v_sub_f32_e32 v107, v107, v52
	v_sub_f32_e32 v106, v106, v52
	v_sub_f32_e32 v105, v105, v52
	v_sub_f32_e32 v104, v104, v52
	v_sub_f32_e32 v103, v103, v52
	v_sub_f32_e32 v102, v102, v52
	v_sub_f32_e32 v101, v101, v52
	v_sub_f32_e32 v100, v100, v52
	v_sub_f32_e32 v83, v83, v52
	v_sub_f32_e32 v82, v82, v52
	v_sub_f32_e32 v81, v81, v52
	v_sub_f32_e32 v80, v80, v52
	v_sub_f32_e32 v79, v79, v52
	v_sub_f32_e32 v78, v78, v52
	v_sub_f32_e32 v77, v77, v52
	v_sub_f32_e32 v76, v76, v52
	v_sub_f32_e32 v75, v75, v52
	v_sub_f32_e32 v74, v74, v52
	v_sub_f32_e32 v73, v73, v52
	v_sub_f32_e32 v72, v72, v52
	v_sub_f32_e32 v71, v71, v52
	v_sub_f32_e32 v70, v70, v52
	v_sub_f32_e32 v69, v69, v52
	v_sub_f32_e32 v68, v68, v52
	v_sub_f32_e32 v51, v51, v52
	v_sub_f32_e32 v50, v50, v52
	v_sub_f32_e32 v49, v49, v52
	v_sub_f32_e32 v48, v48, v52
	v_sub_f32_e32 v47, v47, v52
	v_sub_f32_e32 v46, v46, v52
	v_sub_f32_e32 v45, v45, v52
	v_sub_f32_e32 v44, v44, v52
	v_sub_f32_e32 v43, v43, v52
	v_sub_f32_e32 v42, v42, v52
	v_sub_f32_e32 v41, v41, v52
	v_sub_f32_e32 v40, v40, v52
	v_sub_f32_e32 v39, v39, v52
	v_sub_f32_e32 v38, v38, v52
	v_sub_f32_e32 v37, v37, v52
	v_sub_f32_e32 v36, v36, v52

.LBB0_1464:
	s_add_i32 s79, s79, 2
	s_and_b32 s2, s79, 2
	s_mulk_i32 s2, 0x3000
	v_add_u32_e32 v56, s2, v168
	v_add_u32_e32 v248, s2, v244
	v_add_u32_e32 v249, s2, v245
	v_add_u32_e32 v250, s2, v246
	v_add_u32_e32 v251, s2, v247
	ds_read_b128 v[52:55], v248
	ds_read_b128 v[172:175], v248 offset:4096
	ds_read_b128 v[176:179], v249
	ds_read_b128 v[180:183], v249 offset:4096
	ds_read_b128 v[184:187], v250
	ds_read_b128 v[190:193], v250 offset:4096
	ds_read_b128 v[212:215], v251
	ds_read_b128 v[216:219], v251 offset:4096
	ds_read_b128 v[224:227], v56 offset:8192
	ds_read_b128 v[228:231], v56 offset:8704
	ds_read_b128 v[232:235], v56 offset:10240
	ds_read_b128 v[236:239], v56 offset:10752
	s_waitcnt lgkmcnt(11)
	v_mfma_f32_32x32x16_bf16 v[84:99], v[52:55], v[116:119], v[36:51]
	v_exp_f32_e32 v100, v100
	v_exp_f32_e32 v101, v101
	v_exp_f32_e32 v102, v102
	v_exp_f32_e32 v103, v103
	s_waitcnt lgkmcnt(10)
	v_mfma_f32_32x32x16_bf16 v[52:67], v[172:175], v[116:119], v[36:51]
	v_add_f32_e64 v172, v100, 0
	v_add_f32_e64 v173, v101, 0
	v_add_f32_e64 v172, v102, v172
	v_add_f32_e64 v173, v103, v173
	s_waitcnt lgkmcnt(9)
	v_mfma_f32_32x32x16_bf16 v[84:99], v[176:179], v[120:123], v[84:99]
	v_exp_f32_e32 v104, v104
	v_exp_f32_e32 v105, v105
	v_exp_f32_e32 v106, v106
	v_exp_f32_e32 v107, v107
	v_pk_add_f32 v[172:173], v[104:105], v[172:173]
	s_nop 0
	v_pk_add_f32 v[172:173], v[106:107], v[172:173]
	s_waitcnt lgkmcnt(8)
	v_mfma_f32_32x32x16_bf16 v[52:67], v[180:183], v[120:123], v[52:67]
	s_waitcnt lgkmcnt(7)
	v_mfma_f32_32x32x16_bf16 v[84:99], v[184:187], v[124:127], v[84:99]
	v_exp_f32_e32 v108, v108
	v_exp_f32_e32 v109, v109
	v_exp_f32_e32 v110, v110
	v_exp_f32_e32 v111, v111
	v_pk_add_f32 v[172:173], v[108:109], v[172:173]
	s_nop 0
	v_pk_add_f32 v[172:173], v[110:111], v[172:173]
	s_waitcnt lgkmcnt(6)
	v_mfma_f32_32x32x16_bf16 v[52:67], v[190:193], v[124:127], v[52:67]
	s_waitcnt lgkmcnt(5)
	v_mfma_f32_32x32x16_bf16 v[84:99], v[212:215], v[128:131], v[84:99]
	v_exp_f32_e32 v112, v112
	v_exp_f32_e32 v113, v113
	v_exp_f32_e32 v114, v114
	v_exp_f32_e32 v115, v115
	v_pk_add_f32 v[172:173], v[112:113], v[172:173]
	s_nop 0
	v_pk_add_f32 v[172:173], v[114:115], v[172:173]
	s_waitcnt lgkmcnt(4)
	v_mfma_f32_32x32x16_bf16 v[52:67], v[216:219], v[128:131], v[52:67]
	v_exp_f32_e32 v174, v68
	v_exp_f32_e32 v175, v69
	s_waitcnt lgkmcnt(3)
	v_mfma_f32_32x32x16_bf16 v[84:99], v[224:227], v[132:135], v[84:99]
	v_add_f32_e64 v68, v174, v172
	v_add_f32_e64 v69, v175, v173
	v_exp_f32_e32 v172, v70
	v_exp_f32_e32 v173, v71
	s_nop 0
	v_pk_add_f32 v[68:69], v[172:173], v[68:69]
	s_waitcnt lgkmcnt(2)
	v_mfma_f32_32x32x16_bf16 v[52:67], v[228:231], v[132:135], v[52:67]
	s_waitcnt lgkmcnt(1)
	v_mfma_f32_32x32x16_bf16 v[84:99], v[232:235], v[136:139], v[84:99]
	v_exp_f32_e32 v176, v72
	v_exp_f32_e32 v177, v73
	v_exp_f32_e32 v178, v74
	v_exp_f32_e32 v179, v75
	v_pk_add_f32 v[68:69], v[176:177], v[68:69]
	s_nop 0
	v_pk_add_f32 v[194:195], v[178:179], v[68:69]
	s_waitcnt lgkmcnt(0)
	v_mfma_f32_32x32x16_bf16 v[52:67], v[236:239], v[136:139], v[52:67]
	s_add_i32 s2, s78, 0x2000
	s_and_b32 s2, s2, 0x6000
	v_cvt_pk_bf16_f32 v70, v104, v105
	v_add_u32_e32 v212, s2, v2
	ds_read_b64_tr_b16 v[104:105],v212 offset:0
	v_cvt_pk_bf16_f32 v71, v106, v107
	ds_read_b64_tr_b16 v[106:107],v212 offset:512
	v_cvt_pk_bf16_f32 v72, v108, v109
	ds_read_b64_tr_b16 v[108:109],v212 offset:1024
	v_cvt_pk_bf16_f32 v73, v110, v111
	ds_read_b64_tr_b16 v[110:111],v212 offset:1536
	v_cvt_pk_bf16_f32 v74, v112, v113
	ds_read_b64_tr_b16 v[112:113],v212 offset:2048
	v_cvt_pk_bf16_f32 v75, v114, v115
	ds_read_b64_tr_b16 v[114:115],v212 offset:2560
	v_cvt_pk_bf16_f32 v68, v100, v101
	v_cvt_pk_bf16_f32 v101, v172, v173
	ds_read_b64_tr_b16 v[172:173],v212 offset:3072
	v_cvt_pk_bf16_f32 v100, v174, v175
	ds_read_b64_tr_b16 v[174:175],v212 offset:3584
	v_cvt_pk_bf16_f32 v69, v102, v103
	v_cvt_pk_bf16_f32 v102, v176, v177
	ds_read_b64_tr_b16 v[176:177],v212 offset:4096
	v_cvt_pk_bf16_f32 v103, v178, v179
	ds_read_b64_tr_b16 v[178:179],v212 offset:4608
	ds_read_b64_tr_b16 v[180:181],v212 offset:5120
	ds_read_b64_tr_b16 v[182:183],v212 offset:5632
	ds_read_b64_tr_b16 v[184:185],v212 offset:6144
	ds_read_b64_tr_b16 v[186:187],v212 offset:6656
	ds_read_b64_tr_b16 v[190:191],v212 offset:7168
	ds_read_b64_tr_b16 v[192:193],v212 offset:7680
	s_waitcnt lgkmcnt(0)
	v_mfma_f32_32x32x16_bf16 v[4:19], v[68:71], v[104:107], v[4:19]
	v_mfma_f32_32x32x16_bf16 v[20:35], v[68:71], v[176:179], v[20:35]
	v_exp_f32_e32 v68, v76
	v_exp_f32_e32 v69, v77
	v_exp_f32_e32 v76, v78
	v_exp_f32_e32 v77, v79
	v_pk_add_f32 v[70:71], v[68:69], v[194:195]
	s_nop 0
	v_pk_add_f32 v[70:71], v[76:77], v[70:71]
	v_mfma_f32_32x32x16_bf16 v[4:19], v[72:75], v[108:111], v[4:19]
	v_cvt_pk_bf16_f32 v68, v68, v69
	v_cvt_pk_bf16_f32 v69, v76, v77
	v_mfma_f32_32x32x16_bf16 v[20:35], v[72:75], v[180:183], v[20:35]
	v_exp_f32_e32 v72, v80
	v_exp_f32_e32 v73, v81
	v_exp_f32_e32 v74, v82
	v_exp_f32_e32 v75, v83
	v_pk_add_f32 v[70:71], v[72:73], v[70:71]
	s_nop 0
	v_pk_add_f32 v[78:79], v[74:75], v[70:71]
	v_cvt_pk_bf16_f32 v70, v72, v73
	v_add_f32_e32 v72, v78, v79
	v_add_f32_e32 v171, v171, v72
	v_cvt_pk_bf16_f32 v71, v74, v75
	v_mfma_f32_32x32x16_bf16 v[4:19], v[100:103], v[112:115], v[4:19]
	v_max3_f32 v72, v84, v52, v85
	s_nop 0
	v_max3_f32 v72, v72, v53, v86
	s_nop 0
	v_max3_f32 v72, v72, v54, v87
	s_nop 0
	v_max3_f32 v72, v72, v55, v88
	v_mfma_f32_32x32x16_bf16 v[20:35], v[100:103], v[184:187], v[20:35]
	v_max3_f32 v72, v72, v56, v89
	s_nop 0
	v_max3_f32 v72, v72, v57, v90
	s_nop 0
	v_max3_f32 v72, v72, v58, v91
	s_nop 0
	v_max3_f32 v72, v72, v59, v91
	v_mfma_f32_32x32x16_bf16 v[4:19], v[68:71], v[172:175], v[4:19]
	v_mfma_f32_32x32x16_bf16 v[20:35], v[68:71], v[190:193], v[20:35]
	v_max3_f32 v68, v72, v92, v60
	s_nop 0
	v_max3_f32 v68, v68, v93, v61
	s_nop 0
	v_max3_f32 v68, v68, v94, v62
	s_nop 0
	v_max3_f32 v68, v68, v95, v63
	s_nop 0
	v_max3_f32 v68, v68, v96, v64
	s_nop 0
	v_max3_f32 v68, v68, v97, v65
	s_nop 0
	v_max3_f32 v68, v68, v98, v66
	s_nop 0
	v_max3_f32 v68, v68, v99, v67
	s_nop 0
	v_mov_b32_e32 v69, v68
	s_nop 1
	v_permlane32_swap_b32_e32 v68, v69
	s_andn2_b64 vcc, exec, s[62:63]
	s_cbranch_vccnz .LBB0_1451
	v_max_f32_e32 v68, v68, v68
	v_max_f32_e32 v69, v69, v69
	v_max_f32_e32 v68, v68, v69
	v_cmp_lt_f32_e32 vcc, s13, v68
	s_cbranch_vccz .LBB0_1451
	v_max_f32_e32 v68, v68, v68
	v_max_f32_e32 v68, 0, v68
	v_exp_f32_e64 v69, -v68
	s_and_saveexec_b64 s[6:7], s[36:37]
	s_cbranch_execz .LBB0_1450
	ds_write_b32 v170, v69
	s_branch .LBB0_1450
